# sload2
# baseline (speedup 1.0000x reference)
.LBB0_23:
	s_and_b64 vcc, exec, s[4:5]
	s_cbranch_vccz .LBB0_358
	s_load_dwordx4 s[12:15], s[0:1], 0x28
	s_load_dwordx2 s[4:5], s[0:1], 0x38
	s_load_dwordx2 s[24:25], s[0:1], 0x48
	s_lshl_b32 s3, s2, 2
	s_addk_i32 s3, 0xf7a8
	v_lshrrev_b32_e32 v1, 6, v0
	v_or_b32_e32 v2, s3, v1
	v_ashrrev_i32_e32 v3, 31, v2
	v_and_b32_e32 v7, 63, v0
	v_lshlrev_b64 v[4:5], 7, v[2:3]
	v_or_b32_e32 v4, v4, v7
	v_lshlrev_b64 v[12:13], 2, v[4:5]
	s_waitcnt lgkmcnt(0)
	v_lshl_add_u64 v[8:9], s[12:13], 0, v[12:13]
	global_load_dword v10, v[8:9], off nt
	global_load_dword v11, v[8:9], off offset:256 nt
	v_lshl_add_u64 v[14:15], s[14:15], 0, v[12:13]
	v_lshl_add_u64 v[12:13], s[4:5], 0, v[12:13]
	global_load_dword v9, v[14:15], off nt
	global_load_dword v8, v[14:15], off offset:256 nt
	global_load_dword v1, v[12:13], off nt
	global_load_dword v6, v[12:13], off offset:256 nt
	s_mov_b32 s3, 0xbfb8aa3b
	s_waitcnt vmcnt(5)
	v_add_f32_e32 v10, 0xc1200000, v10
	v_mul_f32_e64 v12, |v10|, s3
	v_exp_f32_e32 v13, v12
	s_mov_b32 s3, 0x3c23d70a
	v_cmp_ngt_f32_e32 vcc, s3, v13
	s_and_saveexec_b64 s[4:5], vcc
	s_xor_b64 s[10:11], exec, s[4:5]
	s_cbranch_execz .LBB0_26
	v_add_f32_e32 v12, 1.0, v13
	s_mov_b32 s3, 0x800000
	v_cmp_gt_f32_e32 vcc, s3, v12
	s_mov_b32 s3, 0x3f317217
	s_nop 0
	v_cndmask_b32_e64 v13, 0, 32, vcc
	v_ldexp_f32 v12, v12, v13
	v_log_f32_e32 v12, v12
	s_nop 0
	v_mul_f32_e32 v13, 0x3f317217, v12
	v_fma_f32 v13, v12, s3, -v13
	v_fmamk_f32 v13, v12, 0x3377d1cf, v13
	s_mov_b32 s3, 0x7f800000
	v_fmac_f32_e32 v13, 0x3f317217, v12
	v_cmp_lt_f32_e64 s[4:5], |v12|, s3
	s_nop 1
	v_cndmask_b32_e64 v12, v12, v13, s[4:5]
	v_mov_b32_e32 v13, 0x41b17218
	v_cndmask_b32_e32 v13, 0, v13, vcc
	v_sub_f32_e32 v12, v12, v13

_Z13render_kernelPKfPKhS0_S0_Pf:
	s_load_dwordx4 s[4:7], s[0:1], 0x0
	s_load_dwordx2 s[12:13], s[0:1], 0x18
	s_load_dwordx2 s[22:23], s[0:1], 0x10
	v_and_b32_e32 v220, 63, v0
	v_lshrrev_b32_e32 v1, 6, v0
	v_lshlrev_b32_e32 v2, 4, v220
	v_mov_b32_e32 v3, 0
	s_waitcnt lgkmcnt(0)
	v_lshl_add_u64 v[4:5], s[6:7], 0, v[2:3]
	v_lshlrev_b32_e32 v2, 10, v1
	v_add_u32_e32 v10, 0, v2
	v_add_u32_e32 v11, 0x2000, v10
	v_readfirstlane_b32 s3, v10
	v_lshl_add_u64 v[6:7], v[4:5], 0, v[2:3]
	s_mov_b32 m0, s3
	s_mov_b64 s[8:9], 0x2000
	v_readfirstlane_b32 s3, v11
	global_load_lds_dwordx4 v[6:7], off
	v_lshl_add_u64 v[8:9], v[6:7], 0, s[8:9]
	s_mov_b32 m0, s3
	v_add_u32_e32 v11, 0x4000, v10
	global_load_lds_dwordx4 v[8:9], off
	v_or_b32_e32 v8, 0x4000, v2
	v_mov_b32_e32 v9, v3
	v_readfirstlane_b32 s3, v11
	v_add_u32_e32 v11, 0x6000, v10
	v_lshl_add_u64 v[8:9], v[4:5], 0, v[8:9]
	s_mov_b32 m0, s3
	s_mov_b64 s[8:9], 0x6000
	v_readfirstlane_b32 s3, v11
	global_load_lds_dwordx4 v[8:9], off
	v_lshl_add_u64 v[8:9], v[6:7], 0, s[8:9]
	s_mov_b32 m0, s3
	v_add_u32_e32 v11, 0x8000, v10
	global_load_lds_dwordx4 v[8:9], off
	v_or_b32_e32 v8, 0x8000, v2
	v_mov_b32_e32 v9, v3
	v_readfirstlane_b32 s3, v11
	v_add_u32_e32 v11, 0xa000, v10
	v_lshl_add_u64 v[8:9], v[4:5], 0, v[8:9]
	s_mov_b32 m0, s3
	s_mov_b64 s[8:9], 0xa000
	v_readfirstlane_b32 s3, v11
	global_load_lds_dwordx4 v[8:9], off
	v_lshl_add_u64 v[8:9], v[6:7], 0, s[8:9]
	s_mov_b32 m0, s3
	v_add_u32_e32 v11, 0xc000, v10
	global_load_lds_dwordx4 v[8:9], off
	v_or_b32_e32 v8, 0xc000, v2
	v_mov_b32_e32 v9, v3
	v_readfirstlane_b32 s3, v11
	v_add_u32_e32 v11, 0xe000, v10
	v_lshl_add_u64 v[8:9], v[4:5], 0, v[8:9]
	s_mov_b32 m0, s3
	s_mov_b64 s[8:9], 0xe000
	v_readfirstlane_b32 s3, v11
	global_load_lds_dwordx4 v[8:9], off
	v_lshl_add_u64 v[8:9], v[6:7], 0, s[8:9]
	s_mov_b32 m0, s3
	s_mov_b64 s[8:9], 0x12000
	global_load_lds_dwordx4 v[8:9], off
	v_or_b32_e32 v8, 0x10000, v2
	v_add_u32_e32 v11, 0, v8
	v_mov_b32_e32 v9, v3
	v_readfirstlane_b32 s3, v11
	v_lshl_add_u64 v[8:9], v[4:5], 0, v[8:9]
	s_mov_b32 m0, s3
	v_lshl_add_u64 v[6:7], v[6:7], 0, s[8:9]
	global_load_lds_dwordx4 v[8:9], off
	v_add_u32_e32 v8, 0x12000, v10
	s_nop 0
	v_readfirstlane_b32 s3, v8
	s_mov_b32 m0, s3
	s_movk_i32 s3, 0x58
	global_load_lds_dwordx4 v[6:7], off
	v_or_b32_e32 v6, 0x50, v1
	v_cmp_gt_u32_e32 vcc, s3, v6
	s_and_saveexec_b64 s[8:9], vcc
	s_cbranch_execz .LBB1_2
	v_lshlrev_b32_e32 v6, 10, v6
	v_mov_b32_e32 v7, v3
	v_add_u32_e32 v3, 0, v6
	v_lshl_add_u64 v[4:5], v[4:5], 0, v[6:7]
	v_readfirstlane_b32 s3, v3
	s_mov_b32 m0, s3
	s_nop 0
	global_load_lds_dwordx4 v[4:5], off
.LBB1_2:
	s_or_b64 exec, exec, s[8:9]
	s_load_dwordx2 s[8:9], s[0:1], 0x20
	s_movk_i32 s3, 0x80
	v_cmp_gt_u32_e32 vcc, s3, v0
	s_and_saveexec_b64 s[10:11], vcc
	s_cbranch_execz .LBB1_4
	v_lshlrev_b32_e32 v3, 2, v0
	s_waitcnt lgkmcnt(0)
	global_load_dword v4, v3, s[22:23]
	v_add_u32_e32 v3, 0, v3
	v_add_u32_e32 v3, 0x18000, v3
	s_waitcnt vmcnt(0)
	v_mul_f32_e32 v4, 0xf800000, v4
	ds_write_b32 v3, v4

	.amdhsa_kernel _Z13render_kernelPKfPKhS0_S0_Pf
		.amdhsa_group_segment_fixed_size 0
		.amdhsa_private_segment_fixed_size 0
		.amdhsa_kernarg_size 40
		.amdhsa_user_sgpr_count 2
		.amdhsa_user_sgpr_dispatch_ptr 0
		.amdhsa_user_sgpr_queue_ptr 0
		.amdhsa_user_sgpr_kernarg_segment_ptr 1
		.amdhsa_user_sgpr_dispatch_id 0
		.amdhsa_user_sgpr_kernarg_preload_length 0
		.amdhsa_user_sgpr_kernarg_preload_offset 0
		.amdhsa_user_sgpr_private_segment_size 0
		.amdhsa_uses_dynamic_stack 0
		.amdhsa_enable_private_segment 0
		.amdhsa_system_sgpr_workgroup_id_x 1
		.amdhsa_system_sgpr_workgroup_id_y 0
		.amdhsa_system_sgpr_workgroup_id_z 0
		.amdhsa_system_sgpr_workgroup_info 0
		.amdhsa_system_vgpr_workitem_id 0
		.amdhsa_next_free_vgpr 256
		.amdhsa_next_free_sgpr 24
		.amdhsa_accum_offset 256
		.amdhsa_reserve_vcc 1
		.amdhsa_float_round_mode_32 0
		.amdhsa_float_round_mode_16_64 0
		.amdhsa_float_denorm_mode_32 3
		.amdhsa_float_denorm_mode_16_64 3
		.amdhsa_dx10_clamp 1
		.amdhsa_ieee_mode 1
		.amdhsa_fp16_overflow 0
		.amdhsa_tg_split 0
		.amdhsa_exception_fp_ieee_invalid_op 0
		.amdhsa_exception_fp_denorm_src 0
		.amdhsa_exception_fp_ieee_div_zero 0
		.amdhsa_exception_fp_ieee_overflow 0
		.amdhsa_exception_fp_ieee_underflow 0
		.amdhsa_exception_fp_ieee_inexact 0
		.amdhsa_exception_int_div_zero 0
	.end_amdhsa_kernel

amdhsa.kernels:
  - .agpr_count:     0
    .args:
      - .actual_access:  read_only
        .address_space:  global
        .offset:         0
        .size:           8
        .value_kind:     global_buffer
      - .actual_access:  read_only
        .address_space:  global
        .offset:         8
        .size:           8
        .value_kind:     global_buffer
      - .actual_access:  read_only
        .address_space:  global
        .offset:         16
        .size:           8
        .value_kind:     global_buffer
      - .actual_access:  read_only
        .address_space:  global
        .offset:         24
        .size:           8
        .value_kind:     global_buffer
      - .actual_access:  read_only
        .address_space:  global
        .offset:         32
        .size:           8
        .value_kind:     global_buffer
      - .actual_access:  read_only
        .address_space:  global
        .offset:         40
        .size:           8
        .value_kind:     global_buffer
      - .actual_access:  read_only
        .address_space:  global
        .offset:         48
        .size:           8
        .value_kind:     global_buffer
      - .actual_access:  read_only
        .address_space:  global
        .offset:         56
        .size:           8
        .value_kind:     global_buffer
      - .actual_access:  write_only
        .address_space:  global
        .offset:         64
        .size:           8
        .value_kind:     global_buffer
      - .actual_access:  write_only
        .address_space:  global
        .offset:         72
        .size:           8
        .value_kind:     global_buffer
    .group_segment_fixed_size: 1280
    .kernarg_segment_align: 8
    .kernarg_segment_size: 80
    .language:       OpenCL C
    .language_version:
      - 2
      - 0
    .max_flat_workgroup_size: 256
    .name:           _Z11prep_kernelPKfS0_S0_S0_S0_S0_S0_S0_PhPf
    .private_segment_fixed_size: 0
    .sgpr_count:     32
    .sgpr_spill_count: 0
    .symbol:         _Z11prep_kernelPKfS0_S0_S0_S0_S0_S0_S0_PhPf.kd
    .uniform_work_group_size: 1
    .uses_dynamic_stack: false
    .vgpr_count:     72
    .vgpr_spill_count: 0
    .wavefront_size: 64
  - .agpr_count:     0
    .args:
      - .actual_access:  read_only
        .address_space:  global
        .offset:         0
        .size:           8
        .value_kind:     global_buffer
      - .address_space:  global
        .offset:         8
        .size:           8
        .value_kind:     global_buffer
      - .actual_access:  read_only
        .address_space:  global
        .offset:         16
        .size:           8
        .value_kind:     global_buffer
      - .actual_access:  read_only
        .address_space:  global
        .offset:         24
        .size:           8
        .value_kind:     global_buffer
      - .actual_access:  write_only
        .address_space:  global
        .offset:         32
        .size:           8
        .value_kind:     global_buffer
    .group_segment_fixed_size: 0
    .kernarg_segment_align: 8
    .kernarg_segment_size: 40
    .language:       OpenCL C
    .language_version:
      - 2
      - 0
    .max_flat_workgroup_size: 512
    .name:           _Z13render_kernelPKfPKhS0_S0_Pf
    .private_segment_fixed_size: 0
    .sgpr_count:     30
    .sgpr_spill_count: 0
    .symbol:         _Z13render_kernelPKfPKhS0_S0_Pf.kd
    .uniform_work_group_size: 1
    .uses_dynamic_stack: false
    .vgpr_count:     256
    .vgpr_spill_count: 0
    .wavefront_size: 64
